# phase 3 w_in GEMM: staggered (un-aligned) epilogue protocol instead of the aligned one (short bf16-store epilogue)
# baseline (speedup 1.0000x reference)
.LBB0_457:
	s_and_b64 vcc, exec, s[60:61]
	s_cbranch_vccz .LBB0_459
.LBB0_459:
	s_lshl_b32 s1, s84, 10
	v_mbcnt_lo_u32_b32 v138, -1, 0
	v_mbcnt_hi_u32_b32 v138, -1, v138
	s_add_i32 s1, s1, 0
	v_and_or_b32 v0, v138, 15, s79
	v_lshl_add_u32 v130, v0, 2, s1
	v_add_u32_e32 v130, 0x23000, v130
	ds_read2_b32 v[136:137], v130 offset1:16
	ds_read2_b32 v[134:135], v130 offset0:32 offset1:48
	ds_read2_b32 v[132:133], v130 offset0:128 offset1:144
	ds_read2_b32 v[130:131], v130 offset0:160 offset1:176
	v_ashrrev_i32_e32 v149, 4, v138
	s_cmp_lg_u32 s0, 20
	s_mov_b64 s[26:27], -1
	s_cbranch_scc0 .LBB0_461
	s_mul_i32 s2, s88, 0x2a0000
	s_mul_hi_i32 s1, s88, 0x2a0000
	s_add_u32 s2, s75, s2
	s_addc_u32 s11, s76, s1
	s_lshl_b32 s0, s0, 8
	s_ashr_i32 s1, s0, 31
	s_lshl_b64 s[0:1], s[0:1], 1
	s_add_u32 s0, s2, s0
	s_addc_u32 s1, s11, s1
	v_lshl_add_u32 v138, v149, 3, s80
	v_mov_b64_e32 v[150:151], s[0:1]
	v_mad_i64_i32 v[150:151], s[0:1], v0, s33, v[150:151]
	v_ashrrev_i32_e32 v139, 31, v138
	v_lshl_add_u64 v[138:139], v[138:139], 1, v[150:151]
	s_waitcnt lgkmcnt(0)
	v_pk_mul_f32 v[152:153], v[68:69], v[136:137] op_sel_hi:[1,0]
	v_pk_mul_f32 v[150:151], v[66:67], v[136:137] op_sel_hi:[1,0]
	v_pk_mul_f32 v[156:157], v[70:71], v[136:137] op_sel_hi:[1,0]
	v_pk_mul_f32 v[154:155], v[72:73], v[136:137] op_sel_hi:[1,0]
	v_cvt_pk_bf16_f32 v150, v150, v151
	v_cvt_pk_bf16_f32 v151, v152, v153
	v_cvt_pk_bf16_f32 v152, v156, v157
	s_mov_b64 s[14:15], 0x2a000
	v_cvt_pk_bf16_f32 v153, v154, v155
	v_mov_b32_e32 v156, v137
	global_store_dwordx4 v[138:139], v[150:153], off
	v_lshl_add_u64 v[154:155], v[138:139], 0, s[14:15]
	v_pk_mul_f32 v[158:159], v[64:65], v[156:157] op_sel_hi:[1,0]
	v_pk_mul_f32 v[152:153], v[60:61], v[156:157] op_sel_hi:[1,0]
	v_pk_mul_f32 v[150:151], v[58:59], v[156:157] op_sel_hi:[1,0]
	v_pk_mul_f32 v[160:161], v[62:63], v[156:157] op_sel_hi:[1,0]
	v_cvt_pk_bf16_f32 v150, v150, v151
	v_cvt_pk_bf16_f32 v151, v152, v153
	s_mov_b64 s[20:21], 0xa8000
	v_cvt_pk_bf16_f32 v152, v160, v161
	v_cvt_pk_bf16_f32 v153, v158, v159
	global_store_dwordx4 v[154:155], v[150:153], off
	v_lshl_add_u64 v[154:155], v[154:155], 0, s[14:15]
	v_pk_mul_f32 v[158:159], v[56:57], v[134:135] op_sel_hi:[1,0]
	v_pk_mul_f32 v[152:153], v[52:53], v[134:135] op_sel_hi:[1,0]
	v_pk_mul_f32 v[150:151], v[50:51], v[134:135] op_sel_hi:[1,0]
	v_pk_mul_f32 v[160:161], v[54:55], v[134:135] op_sel_hi:[1,0]
	v_cvt_pk_bf16_f32 v150, v150, v151
	v_cvt_pk_bf16_f32 v151, v152, v153
	v_pk_mul_f32 v[128:129], v[128:129], v[136:137] op_sel_hi:[1,0]
	v_cvt_pk_bf16_f32 v152, v160, v161
	v_cvt_pk_bf16_f32 v153, v158, v159
	v_mov_b32_e32 v158, v135
	global_store_dwordx4 v[154:155], v[150:153], off
	v_lshl_add_u64 v[154:155], v[154:155], 0, s[14:15]
	v_pk_mul_f32 v[160:161], v[48:49], v[158:159] op_sel_hi:[1,0]
	v_pk_mul_f32 v[150:151], v[42:43], v[158:159] op_sel_hi:[1,0]
	v_pk_mul_f32 v[152:153], v[44:45], v[158:159] op_sel_hi:[1,0]
	v_cvt_pk_bf16_f32 v150, v150, v151
	v_pk_mul_f32 v[162:163], v[46:47], v[158:159] op_sel_hi:[1,0]
	v_cvt_pk_bf16_f32 v151, v152, v153
	v_pk_mul_f32 v[126:127], v[126:127], v[136:137] op_sel_hi:[1,0]
	v_cvt_pk_bf16_f32 v152, v162, v163
	v_cvt_pk_bf16_f32 v153, v160, v161
	global_store_dwordx4 v[154:155], v[150:153], off
	v_pk_mul_f32 v[160:161], v[32:33], v[132:133] op_sel_hi:[1,0]
	v_pk_mul_f32 v[162:163], v[30:31], v[132:133] op_sel_hi:[1,0]
	v_lshl_add_u64 v[150:151], v[154:155], 0, s[14:15]
	v_pk_mul_f32 v[152:153], v[28:29], v[132:133] op_sel_hi:[1,0]
	v_lshl_add_u64 v[154:155], v[150:151], 0, s[20:21]
	v_pk_mul_f32 v[150:151], v[26:27], v[132:133] op_sel_hi:[1,0]
	s_mov_b64 s[0:1], 0x2a100
	v_cvt_pk_bf16_f32 v150, v150, v151
	v_cvt_pk_bf16_f32 v151, v152, v153
	v_cvt_pk_bf16_f32 v152, v162, v163
	v_cvt_pk_bf16_f32 v153, v160, v161
	v_mov_b32_e32 v160, v133
	global_store_dwordx4 v[154:155], v[150:153], off
	v_lshl_add_u64 v[154:155], v[154:155], 0, s[14:15]
	v_pk_mul_f32 v[162:163], v[24:25], v[160:161] op_sel_hi:[1,0]
	v_pk_mul_f32 v[152:153], v[20:21], v[160:161] op_sel_hi:[1,0]
	v_pk_mul_f32 v[150:151], v[18:19], v[160:161] op_sel_hi:[1,0]
	v_pk_mul_f32 v[164:165], v[22:23], v[160:161] op_sel_hi:[1,0]
	v_cvt_pk_bf16_f32 v150, v150, v151
	v_cvt_pk_bf16_f32 v151, v152, v153
	v_pk_mul_f32 v[120:121], v[120:121], v[156:157] op_sel_hi:[1,0]
	v_cvt_pk_bf16_f32 v152, v164, v165
	v_cvt_pk_bf16_f32 v153, v162, v163
	global_store_dwordx4 v[154:155], v[150:153], off
	v_lshl_add_u64 v[154:155], v[154:155], 0, s[14:15]
	v_pk_mul_f32 v[162:163], v[16:17], v[130:131] op_sel_hi:[1,0]
	v_pk_mul_f32 v[152:153], v[12:13], v[130:131] op_sel_hi:[1,0]
	v_pk_mul_f32 v[150:151], v[10:11], v[130:131] op_sel_hi:[1,0]
	v_pk_mul_f32 v[164:165], v[14:15], v[130:131] op_sel_hi:[1,0]
	v_cvt_pk_bf16_f32 v150, v150, v151
	v_cvt_pk_bf16_f32 v151, v152, v153
	v_pk_mul_f32 v[118:119], v[118:119], v[156:157] op_sel_hi:[1,0]
	v_cvt_pk_bf16_f32 v152, v164, v165
	v_cvt_pk_bf16_f32 v153, v162, v163
	v_mov_b32_e32 v162, v131
	global_store_dwordx4 v[154:155], v[150:153], off
	v_lshl_add_u64 v[154:155], v[154:155], 0, s[14:15]
	v_pk_mul_f32 v[164:165], v[8:9], v[162:163] op_sel_hi:[1,0]
	v_pk_mul_f32 v[150:151], v[2:3], v[162:163] op_sel_hi:[1,0]
	v_pk_mul_f32 v[152:153], v[4:5], v[162:163] op_sel_hi:[1,0]
	v_cvt_pk_bf16_f32 v150, v150, v151
	v_pk_mul_f32 v[166:167], v[6:7], v[162:163] op_sel_hi:[1,0]
	v_cvt_pk_bf16_f32 v151, v152, v153
	v_pk_mul_f32 v[112:113], v[112:113], v[134:135] op_sel_hi:[1,0]
	v_cvt_pk_bf16_f32 v152, v166, v167
	v_cvt_pk_bf16_f32 v153, v164, v165
	global_store_dwordx4 v[154:155], v[150:153], off
	v_pk_mul_f32 v[110:111], v[110:111], v[134:135] op_sel_hi:[1,0]
	v_pk_mul_f32 v[96:97], v[96:97], v[158:159] op_sel_hi:[1,0]
	v_lshl_add_u64 v[150:151], v[154:155], 0, s[14:15]
	v_pk_mul_f32 v[94:95], v[94:95], v[158:159] op_sel_hi:[1,0]
	v_lshl_add_u64 v[150:151], v[150:151], 0, s[20:21]
	v_pk_mul_f32 v[98:99], v[98:99], v[132:133] op_sel_hi:[1,0]
	v_pk_mul_f32 v[150:151], v[124:125], v[136:137] op_sel_hi:[1,0]
	v_pk_mul_f32 v[124:125], v[122:123], v[136:137] op_sel_hi:[1,0]
	v_cvt_pk_bf16_f32 v122, v126, v127
	v_cvt_pk_bf16_f32 v123, v128, v129
	v_pk_mul_f32 v[82:83], v[82:83], v[160:161] op_sel_hi:[1,0]
	v_cvt_pk_bf16_f32 v124, v124, v125
	v_cvt_pk_bf16_f32 v125, v150, v151
	global_store_dwordx4 v[138:139], v[122:125], off offset:256
	v_pk_mul_f32 v[84:85], v[84:85], v[160:161] op_sel_hi:[1,0]
	v_pk_mul_f32 v[88:89], v[88:89], v[160:161] op_sel_hi:[1,0]
	v_lshl_add_u64 v[122:123], v[138:139], 0, s[0:1]
	v_pk_mul_f32 v[124:125], v[116:117], v[156:157] op_sel_hi:[1,0]
	v_pk_mul_f32 v[116:117], v[114:115], v[156:157] op_sel_hi:[1,0]
	v_cvt_pk_bf16_f32 v114, v118, v119
	v_cvt_pk_bf16_f32 v115, v120, v121
	v_pk_mul_f32 v[86:87], v[86:87], v[160:161] op_sel_hi:[1,0]
	v_cvt_pk_bf16_f32 v116, v116, v117
	v_cvt_pk_bf16_f32 v117, v124, v125
	global_store_dwordx4 v[122:123], v[114:117], off
	v_pk_mul_f32 v[80:81], v[80:81], v[130:131] op_sel_hi:[1,0]
	v_pk_mul_f32 v[78:79], v[78:79], v[130:131] op_sel_hi:[1,0]
	v_lshl_add_u64 v[114:115], v[122:123], 0, s[14:15]
	v_pk_mul_f32 v[116:117], v[108:109], v[134:135] op_sel_hi:[1,0]
	v_pk_mul_f32 v[108:109], v[106:107], v[134:135] op_sel_hi:[1,0]
	v_cvt_pk_bf16_f32 v106, v110, v111
	v_cvt_pk_bf16_f32 v107, v112, v113
	v_pk_mul_f32 v[34:35], v[34:35], v[162:163] op_sel_hi:[1,0]
	v_cvt_pk_bf16_f32 v108, v108, v109
	v_cvt_pk_bf16_f32 v109, v116, v117
	global_store_dwordx4 v[114:115], v[106:109], off
	v_pk_mul_f32 v[36:37], v[36:37], v[162:163] op_sel_hi:[1,0]
	v_pk_mul_f32 v[40:41], v[40:41], v[162:163] op_sel_hi:[1,0]
	v_lshl_add_u64 v[106:107], v[114:115], 0, s[14:15]
	v_pk_mul_f32 v[108:109], v[92:93], v[158:159] op_sel_hi:[1,0]
	v_pk_mul_f32 v[92:93], v[90:91], v[158:159] op_sel_hi:[1,0]
	v_cvt_pk_bf16_f32 v90, v94, v95
	v_cvt_pk_bf16_f32 v91, v96, v97
	v_pk_mul_f32 v[96:97], v[100:101], v[132:133] op_sel_hi:[1,0]
	v_cvt_pk_bf16_f32 v92, v92, v93
	v_cvt_pk_bf16_f32 v93, v108, v109
	global_store_dwordx4 v[106:107], v[90:93], off
	v_pk_mul_f32 v[38:39], v[38:39], v[162:163] op_sel_hi:[1,0]
	s_nop 0
	v_lshl_add_u64 v[90:91], v[106:107], 0, s[14:15]
	v_pk_mul_f32 v[92:93], v[104:105], v[132:133] op_sel_hi:[1,0]
	v_lshl_add_u64 v[94:95], v[90:91], 0, s[20:21]
	v_pk_mul_f32 v[90:91], v[102:103], v[132:133] op_sel_hi:[1,0]
	s_nop 0
	v_cvt_pk_bf16_f32 v90, v90, v91
	v_cvt_pk_bf16_f32 v91, v92, v93
	v_cvt_pk_bf16_f32 v92, v98, v99
	v_cvt_pk_bf16_f32 v93, v96, v97
	global_store_dwordx4 v[94:95], v[90:93], off
	s_nop 1
	v_lshl_add_u64 v[90:91], v[94:95], 0, s[14:15]
	v_cvt_pk_bf16_f32 v82, v82, v83
	v_cvt_pk_bf16_f32 v83, v84, v85
	v_cvt_pk_bf16_f32 v84, v86, v87
	v_cvt_pk_bf16_f32 v85, v88, v89
	global_store_dwordx4 v[90:91], v[82:85], off
	s_nop 1
	v_lshl_add_u64 v[82:83], v[90:91], 0, s[14:15]
	v_pk_mul_f32 v[84:85], v[76:77], v[130:131] op_sel_hi:[1,0]
	v_pk_mul_f32 v[76:77], v[74:75], v[130:131] op_sel_hi:[1,0]
	v_cvt_pk_bf16_f32 v74, v78, v79
	v_cvt_pk_bf16_f32 v75, v80, v81
	s_nop 0
	v_cvt_pk_bf16_f32 v76, v76, v77
	v_cvt_pk_bf16_f32 v77, v84, v85
	global_store_dwordx4 v[82:83], v[74:77], off
	s_nop 1
	v_lshl_add_u64 v[74:75], v[82:83], 0, s[14:15]
	v_cvt_pk_bf16_f32 v34, v34, v35
	v_cvt_pk_bf16_f32 v35, v36, v37
	v_cvt_pk_bf16_f32 v36, v38, v39
	v_cvt_pk_bf16_f32 v37, v40, v41
	global_store_dwordx4 v[74:75], v[34:37], off
	s_nop 1
	v_lshl_add_u64 v[34:35], v[74:75], 0, s[14:15]
	s_nop 0
	v_lshl_add_u64 v[34:35], v[34:35], 0, s[20:21]
	s_cbranch_execnz .LBB0_465
	s_branch .LBB0_462

.LBB0_465:
	s_and_b64 vcc, exec, s[42:43]
	s_mov_b64 s[26:27], -1
	s_cbranch_vccnz .LBB0_445
	v_mov_b32_e32 v0, v1
	v_mov_b64_e32 v[38:39], v[0:1]
	s_cmp_lg_u32 s87, s88
	s_cselect_b64 s[0:1], -1, 0
	v_mfma_f32_4x4x4_16b_f16 v[66:69], v[38:39], v[38:39], 0 cbsz:4
	v_cndmask_b32_e64 v0, 0, 1, s[0:1]
	v_mfma_f32_4x4x4_16b_f16 v[70:73], v[38:39], v[38:39], 0 cbsz:4 abid:1
	v_readfirstlane_b32 s0, v0
	v_mfma_f32_4x4x4_16b_f16 v[58:61], v[38:39], v[38:39], 0 cbsz:4 abid:2
	s_andn2_b64 vcc, exec, s[52:53]
	v_mfma_f32_4x4x4_16b_f16 v[62:65], v[38:39], v[38:39], 0 cbsz:4 abid:3
	v_mfma_f32_4x4x4_16b_f16 v[50:53], v[38:39], v[38:39], 0 cbsz:4 abid:4
	v_mfma_f32_4x4x4_16b_f16 v[54:57], v[38:39], v[38:39], 0 cbsz:4 abid:5
	v_mfma_f32_4x4x4_16b_f16 v[42:45], v[38:39], v[38:39], 0 cbsz:4 abid:6
	v_mfma_f32_4x4x4_16b_f16 v[46:49], v[38:39], v[38:39], 0 cbsz:4 abid:7
	v_mfma_f32_4x4x4_16b_f16 v[126:129], v[38:39], v[38:39], 0 cbsz:4 abid:8
	v_mfma_f32_4x4x4_16b_f16 v[122:125], v[38:39], v[38:39], 0 cbsz:4 abid:9
	v_mfma_f32_4x4x4_16b_f16 v[118:121], v[38:39], v[38:39], 0 cbsz:4 abid:10
	v_mfma_f32_4x4x4_16b_f16 v[114:117], v[38:39], v[38:39], 0 cbsz:4 abid:11
	v_mfma_f32_4x4x4_16b_f16 v[110:113], v[38:39], v[38:39], 0 cbsz:4 abid:12
	v_mfma_f32_4x4x4_16b_f16 v[106:109], v[38:39], v[38:39], 0 cbsz:4 abid:13
	v_mfma_f32_4x4x4_16b_f16 v[94:97], v[38:39], v[38:39], 0 cbsz:4 abid:14
	v_mfma_f32_4x4x4_16b_f16 v[90:93], v[38:39], v[38:39], 0 cbsz:4 abid:15
	v_mfma_f32_4x4x4_16b_f16 v[26:29], v[38:39], v[38:39], 0 cbsz:4 blgp:1
	v_mfma_f32_4x4x4_16b_f16 v[30:33], v[38:39], v[38:39], 0 cbsz:4 abid:1 blgp:1
	v_mfma_f32_4x4x4_16b_f16 v[18:21], v[38:39], v[38:39], 0 cbsz:4 abid:2 blgp:1
	v_mfma_f32_4x4x4_16b_f16 v[22:25], v[38:39], v[38:39], 0 cbsz:4 abid:3 blgp:1
	v_mfma_f32_4x4x4_16b_f16 v[10:13], v[38:39], v[38:39], 0 cbsz:4 abid:4 blgp:1
	v_mfma_f32_4x4x4_16b_f16 v[14:17], v[38:39], v[38:39], 0 cbsz:4 abid:5 blgp:1
	v_mfma_f32_4x4x4_16b_f16 v[2:5], v[38:39], v[38:39], 0 cbsz:4 abid:6 blgp:1
	v_mfma_f32_4x4x4_16b_f16 v[6:9], v[38:39], v[38:39], 0 cbsz:4 abid:7 blgp:1
	v_mfma_f32_4x4x4_16b_f16 v[102:105], v[38:39], v[38:39], 0 cbsz:4 abid:8 blgp:1
	v_mfma_f32_4x4x4_16b_f16 v[98:101], v[38:39], v[38:39], 0 cbsz:4 abid:9 blgp:1
	v_mfma_f32_4x4x4_16b_f16 v[82:85], v[38:39], v[38:39], 0 cbsz:4 abid:10 blgp:1
	v_mfma_f32_4x4x4_16b_f16 v[86:89], v[38:39], v[38:39], 0 cbsz:4 abid:11 blgp:1
	v_mfma_f32_4x4x4_16b_f16 v[78:81], v[38:39], v[38:39], 0 cbsz:4 abid:12 blgp:1
	v_mfma_f32_4x4x4_16b_f16 v[74:77], v[38:39], v[38:39], 0 cbsz:4 abid:13 blgp:1
	v_mfma_f32_4x4x4_16b_f16 v[34:37], v[38:39], v[38:39], 0 cbsz:4 abid:14 blgp:1
	v_mfma_f32_4x4x4_16b_f16 v[38:41], v[38:39], v[38:39], 0 cbsz:4 abid:15 blgp:1
	s_cbranch_vccnz .LBB0_444
	s_branch .LBB0_444
.LBB0_468:
	s_waitcnt vmcnt(0)
	v_readlane_b32 s46, v255, 10
	s_and_b64 vcc, exec, s[60:61]
	s_cbranch_vccz .Lual_3
	s_barrier
.Lual_3:
	s_barrier
.LBB0_469:
	s_add_u32 s0, s36, 0x3e900000
	s_addc_u32 s1, s37, 0
	s_add_u32 s2, s36, 0x4bb00000
	s_addc_u32 s14, s37, 0
	s_add_u32 s15, s36, 0x8800000
	s_addc_u32 s18, s37, 0
	s_add_u32 s20, s36, 0x4d300000
	s_addc_u32 s25, s37, 0
	s_add_u32 s56, s36, 0x3f900000
	s_addc_u32 s57, s37, 0
	s_add_u32 s58, s36, 0xc800000
	s_addc_u32 s59, s37, 0
	s_mov_b64 s[36:37], -1
	s_mov_b64 s[26:27], 0
	s_branch .LBB0_472
